# v25: v10 + layer-1 expert down-proj weight bf16 conversion removed from phase 16 and interleaved one 32x32 block per wave per row into the rwkv_out row loop on the scan-idle workgroups (loads with the
# speedup vs baseline: 1.0118x; 1.0000x over previous
.Lx14_linit:
	s_barrier
	v_mbcnt_lo_u32_b32 v1, -1, 0
	v_mbcnt_hi_u32_b32 v1, -1, v1
	v_lshlrev_b32_e32 v2, 4, v1
	v_lshrrev_b32_e32 v3, 3, v1
	v_lshlrev_b32_e32 v3, 2, v3
	v_and_b32_e32 v4, 31, v1
	v_lshlrev_b32_e32 v4, 2, v4
	v_lshrrev_b32_e32 v9, 5, v1
	v_lshl_add_u32 v4, v9, 8, v4
	v_lshlrev_b32_e32 v9, 5, v1
	s_load_dwordx4 s[28:31], s[74:75], 0x100
	s_add_u32 s4, s54, 0x8c00000
	s_addc_u32 s5, s55, 0
	s_add_u32 s6, s54, 0x29400000
	s_addc_u32 s7, s55, 0
	s_add_u32 s8, s54, 0x21200000
	s_addc_u32 s9, s55, 0
	s_add_u32 s10, s54, 0x49c00000
	s_addc_u32 s11, s55, 0
	s_add_u32 s12, s54, 0x19000000
	s_addc_u32 s13, s55, 0
	s_add_u32 s14, s54, 0xc00000
	s_addc_u32 s15, s55, 0
	s_add_u32 s16, s54, 0x1000000
	s_addc_u32 s17, s55, 0
	s_add_u32 s20, s54, 0xc400
	s_addc_u32 s21, s55, 0
	s_mov_b32 s18, -1
	s_mov_b32 s19, 0
	s_add_i32 s25, s2, 0xffffff80
	s_lshl_b32 s25, s25, 3
	s_add_i32 s25, s25, s82
	s_and_b32 s40, s25, 15
	s_lshr_b32 s41, s25, 4
	s_lshl_b32 s42, s40, 18
	s_lshl_b32 s43, s41, 7
	s_add_i32 s42, s42, s43
	s_lshl_b32 s43, s41, 15
	s_lshl_b32 s40, s40, 6
	s_add_i32 s43, s43, s40
	s_load_dwordx2 s[44:45], s[74:75], 0x130
	v_lshrrev_b32_e32 v240, 1, v1
	v_and_b32_e32 v241, 1, v1
	v_lshlrev_b32_e32 v242, 13, v240
	v_lshl_add_u32 v242, v241, 6, v242
	v_lshlrev_b32_e32 v243, 10, v240
	v_lshl_add_u32 v243, v241, 5, v243
	v_mul_u32_u24_e32 v244, 0x84, v240
	v_lshl_add_u32 v244, v241, 6, v244
	v_mul_u32_u24_e32 v245, 0x840, v241
	v_lshl_add_u32 v245, v240, 2, v245
	s_mul_i32 s40, s82, 0x1100
	s_add_i32 s40, s40, 0x1000
	v_add_u32_e32 v244, s40, v244
	v_add_u32_e32 v245, s40, v245
	s_lshr_b32 s100, s25, 8
	s_and_b32 s25, s25, 0xff
	s_mov_b32 s24, 0
	s_mov_b32 s26, 0
	s_waitcnt lgkmcnt(0)
	s_add_u32 s44, s44, 0x8000000
	s_addc_u32 s45, s45, 0
	s_add_u32 s44, s44, s42
	s_addc_u32 s45, s45, 0
	s_add_u32 s46, s54, 0x1400000
	s_addc_u32 s47, s55, 0
	s_add_u32 s46, s46, s43
	s_addc_u32 s47, s47, 0
	global_load_dwordx4 v[10:13], v9, s[28:29]
	global_load_dwordx4 v[14:17], v9, s[28:29] offset:16
	global_load_dwordx4 v[18:21], v9, s[28:29] offset:2048
	global_load_dwordx4 v[22:25], v9, s[28:29] offset:2064
	global_load_dwordx4 v[42:45], v9, s[30:31]
	global_load_dwordx4 v[46:49], v9, s[30:31] offset:16
	global_load_dwordx4 v[50:53], v9, s[30:31] offset:2048
	global_load_dwordx4 v[54:57], v9, s[30:31] offset:2064
	v_add_u32_e32 v9, 0x1000, v9
	global_load_dwordx4 v[26:29], v9, s[28:29]
	global_load_dwordx4 v[30:33], v9, s[28:29] offset:16
	global_load_dwordx4 v[34:37], v9, s[28:29] offset:2048
	global_load_dwordx4 v[38:41], v9, s[28:29] offset:2064
	global_load_dwordx4 v[58:61], v9, s[30:31]
	global_load_dwordx4 v[62:65], v9, s[30:31] offset:16
	global_load_dwordx4 v[66:69], v9, s[30:31] offset:2048
	global_load_dwordx4 v[70:73], v9, s[30:31] offset:2064
	s_waitcnt vmcnt(0)
.Lx14_row:
	s_lshr_b32 s0, s24, 2
	s_and_b32 s1, s24, 3
	s_lshl_b32 s0, s0, 10
	s_lshl_b32 s3, s1, 8
	s_add_i32 s0, s0, s3
	s_add_i32 s0, s0, s25
	s_sub_i32 s1, s1, s100
	s_and_b32 s1, s1, 3
	s_lshr_b32 s3, s1, 1
	s_and_b32 s1, s1, 1
	s_sub_i32 s28, 0x1fff, s0
	s_add_i32 s29, s0, 0x2000
	s_cmp_lg_u32 s1, 0
	s_cselect_b32 s28, s29, s28
	s_add_i32 s29, s28, 0x100
	s_lshr_b32 s29, s29, 6
	s_add_i32 s29, s29, 1
	s_sub_i32 s30, 0x40ff, s28
	s_lshr_b32 s30, s30, 6
	s_add_i32 s30, s30, 1
	s_lshl_b32 s31, s3, 14
	s_add_i32 s31, s31, s28
	s_lshl_b32 s3, s3, 7
	v_add_u32_e32 v7, s3, v4
	v_mov_b32_e32 v8, s30
	v_mov_b32_e32 v9, s29
	v_cndmask_b32_e64 v8, v8, v9, s[18:19]
	s_lshl_b32 s0, s31, 12
	v_add_u32_e32 v5, s0, v2
	s_lshl_b32 s1, s31, 7
	v_add_u32_e32 v6, s1, v3
	global_load_dwordx4 v[112:115], v5, s[8:9]
	global_load_dwordx4 v[116:119], v5, s[8:9] offset:1024
	global_load_dwordx4 v[120:123], v5, s[8:9] offset:2048
	global_load_dwordx4 v[124:127], v5, s[8:9] offset:3072
	global_load_dwordx4 v[128:131], v5, s[10:11]
	global_load_dwordx4 v[132:135], v5, s[10:11] offset:1024
	global_load_dwordx4 v[136:139], v5, s[10:11] offset:2048
	global_load_dwordx4 v[140:143], v5, s[10:11] offset:3072
	global_load_dword v144, v6, s[14:15]
	global_load_dword v145, v6, s[14:15] offset:32
	global_load_dword v146, v6, s[14:15] offset:64
	global_load_dword v147, v6, s[14:15] offset:96
	global_load_dword v148, v6, s[16:17]
	global_load_dword v149, v6, s[16:17] offset:32
	global_load_dword v150, v6, s[16:17] offset:64
	global_load_dword v151, v6, s[16:17] offset:96
	s_lshl_b32 s40, s24, 22
	s_add_u32 s40, s44, s40
	s_addc_u32 s41, s45, 0
	global_load_dwordx4 v[200:203], v242, s[40:41] nt
	global_load_dwordx4 v[204:207], v242, s[40:41] offset:16 nt
	global_load_dwordx4 v[208:211], v242, s[40:41] offset:32 nt
	global_load_dwordx4 v[212:215], v242, s[40:41] offset:48 nt
	s_cmp_lg_u32 s26, 0
	s_cbranch_scc1 .Lx14_ready
	s_mov_b32 s27, 0

.Lx14_ready:
	global_load_dwordx4 v[80:83], v5, s[4:5] sc1
	global_load_dwordx4 v[84:87], v5, s[4:5] offset:1024 sc1
	global_load_dwordx4 v[88:91], v5, s[4:5] offset:2048 sc1
	global_load_dwordx4 v[92:95], v5, s[4:5] offset:3072 sc1
	global_load_dwordx4 v[96:99], v5, s[6:7] sc1
	global_load_dwordx4 v[100:103], v5, s[6:7] offset:1024 sc1
	global_load_dwordx4 v[104:107], v5, s[6:7] offset:2048 sc1
	global_load_dwordx4 v[108:111], v5, s[6:7] offset:3072 sc1
	s_waitcnt vmcnt(0)
	ds_write2_b32 v244, v200, v201 offset0:0 offset1:1
	ds_write2_b32 v244, v202, v203 offset0:2 offset1:3
	ds_write2_b32 v244, v204, v205 offset0:4 offset1:5
	ds_write2_b32 v244, v206, v207 offset0:6 offset1:7
	ds_write2_b32 v244, v208, v209 offset0:8 offset1:9
	ds_write2_b32 v244, v210, v211 offset0:10 offset1:11
	ds_write2_b32 v244, v212, v213 offset0:12 offset1:13
	ds_write2_b32 v244, v214, v215 offset0:14 offset1:15
	ds_read_b32 v216, v245
	ds_read_b32 v217, v245 offset:132
	ds_read_b32 v218, v245 offset:264
	ds_read_b32 v219, v245 offset:396
	ds_read_b32 v220, v245 offset:528
	ds_read_b32 v221, v245 offset:660
	ds_read_b32 v222, v245 offset:792
	ds_read_b32 v223, v245 offset:924
	ds_read_b32 v224, v245 offset:1056
	ds_read_b32 v225, v245 offset:1188
	ds_read_b32 v226, v245 offset:1320
	ds_read_b32 v227, v245 offset:1452
	ds_read_b32 v228, v245 offset:1584
	ds_read_b32 v229, v245 offset:1716
	ds_read_b32 v230, v245 offset:1848
	ds_read_b32 v231, v245 offset:1980
	s_lshl_b32 s40, s24, 21
	s_cmp_ge_u32 s24, 25
	s_cselect_b32 s41, 0x1000000, 0
	s_add_i32 s40, s40, s41
	s_add_u32 s40, s46, s40
	s_addc_u32 s41, s47, 0
	s_waitcnt lgkmcnt(0)
	v_cvt_pk_bf16_f32 v232, v216, v217
	v_cvt_pk_bf16_f32 v233, v218, v219
	v_cvt_pk_bf16_f32 v234, v220, v221
	v_cvt_pk_bf16_f32 v235, v222, v223
	v_cvt_pk_bf16_f32 v236, v224, v225
	v_cvt_pk_bf16_f32 v237, v226, v227
	v_cvt_pk_bf16_f32 v238, v228, v229
	v_cvt_pk_bf16_f32 v239, v230, v231
	global_store_dwordx4 v243, v[232:235], s[40:41] nt
	global_store_dwordx4 v243, v[236:239], s[40:41] offset:16 nt
	v_lshlrev_b32_e32 v168, 16, v80
	v_lshlrev_b32_e32 v169, 16, v96
	v_add_f32_e32 v160, v168, v169
	v_and_b32_e32 v168, 0xffff0000, v80
	v_and_b32_e32 v169, 0xffff0000, v96
	v_add_f32_e32 v161, v168, v169
	v_lshlrev_b32_e32 v168, 16, v81
	v_lshlrev_b32_e32 v169, 16, v97
	v_add_f32_e32 v162, v168, v169
	v_and_b32_e32 v168, 0xffff0000, v81
	v_and_b32_e32 v169, 0xffff0000, v97
	v_add_f32_e32 v163, v168, v169
	v_lshlrev_b32_e32 v168, 16, v82
	v_lshlrev_b32_e32 v169, 16, v98
	v_add_f32_e32 v164, v168, v169
	v_and_b32_e32 v168, 0xffff0000, v82
	v_and_b32_e32 v169, 0xffff0000, v98
	v_add_f32_e32 v165, v168, v169
	v_lshlrev_b32_e32 v168, 16, v83
	v_lshlrev_b32_e32 v169, 16, v99
	v_add_f32_e32 v166, v168, v169
	v_and_b32_e32 v168, 0xffff0000, v83
	v_and_b32_e32 v169, 0xffff0000, v99
	v_add_f32_e32 v167, v168, v169
	v_add_f32_e32 v170, v160, v161
	v_add_f32_e32 v170, v170, v162
	v_add_f32_e32 v170, v170, v163
	v_add_f32_e32 v170, v170, v164
	v_add_f32_e32 v170, v170, v165
	v_add_f32_e32 v170, v170, v166
	v_add_f32_e32 v170, v170, v167
	s_nop 1
	v_add_f32_dpp v170, v170, v170 quad_perm:[1,0,3,2] row_mask:0xf bank_mask:0xf bound_ctrl:1
	s_nop 1
	v_add_f32_dpp v170, v170, v170 quad_perm:[2,3,0,1] row_mask:0xf bank_mask:0xf bound_ctrl:1
	s_nop 1
	v_add_f32_dpp v170, v170, v170 row_half_mirror row_mask:0xf bank_mask:0xf bound_ctrl:1
	v_mul_f32_e32 v170, 0x3c800000, v170
	v_sub_f32_e32 v160, v160, v170
	v_sub_f32_e32 v161, v161, v170
	v_sub_f32_e32 v162, v162, v170
	v_sub_f32_e32 v163, v163, v170
	v_sub_f32_e32 v164, v164, v170
	v_sub_f32_e32 v165, v165, v170
	v_sub_f32_e32 v166, v166, v170
	v_sub_f32_e32 v167, v167, v170
	v_mul_f32_e32 v171, v160, v160
	v_fmac_f32_e32 v171, v161, v161
	v_fmac_f32_e32 v171, v162, v162
	v_fmac_f32_e32 v171, v163, v163
	v_fmac_f32_e32 v171, v164, v164
	v_fmac_f32_e32 v171, v165, v165
	v_fmac_f32_e32 v171, v166, v166
	v_fmac_f32_e32 v171, v167, v167
	s_nop 1
	v_add_f32_dpp v171, v171, v171 quad_perm:[1,0,3,2] row_mask:0xf bank_mask:0xf bound_ctrl:1
	s_nop 1
	v_add_f32_dpp v171, v171, v171 quad_perm:[2,3,0,1] row_mask:0xf bank_mask:0xf bound_ctrl:1
	s_nop 1
	v_add_f32_dpp v171, v171, v171 row_half_mirror row_mask:0xf bank_mask:0xf bound_ctrl:1
	v_mov_b32_e32 v172, 0x3a27c5ac
	v_fmac_f32_e32 v172, 0x3c800000, v171
	v_rsq_f32_e32 v172, v172
	v_add_f32_e32 v173, v144, v148
	s_nop 0
	v_mul_f32_e32 v160, v160, v172
	v_mul_f32_e32 v161, v161, v172
	v_mul_f32_e32 v162, v162, v172
	v_mul_f32_e32 v163, v163, v172
	v_mul_f32_e32 v164, v164, v172
	v_mul_f32_e32 v165, v165, v172
	v_mul_f32_e32 v166, v166, v172
	v_mul_f32_e32 v167, v167, v172
	v_fma_f32 v160, v10, v160, v42
	v_fma_f32 v161, v11, v161, v43
	v_fma_f32 v162, v12, v162, v44
	v_fma_f32 v163, v13, v163, v45
	v_fma_f32 v164, v14, v164, v46
	v_fma_f32 v165, v15, v165, v47
	v_fma_f32 v166, v16, v166, v48
	v_fma_f32 v167, v17, v167, v49
	v_lshlrev_b32_e32 v168, 16, v112
	v_fmac_f32_e32 v160, v173, v168
	v_and_b32_e32 v169, 0xffff0000, v112
	v_fmac_f32_e32 v161, v173, v169
	v_lshlrev_b32_e32 v168, 16, v128
	v_mul_f32_e32 v160, v160, v168
	v_and_b32_e32 v169, 0xffff0000, v128
	v_mul_f32_e32 v161, v161, v169
	v_lshlrev_b32_e32 v168, 16, v113
	v_fmac_f32_e32 v162, v173, v168
	v_and_b32_e32 v169, 0xffff0000, v113
	v_fmac_f32_e32 v163, v173, v169
	v_lshlrev_b32_e32 v168, 16, v129
	v_mul_f32_e32 v162, v162, v168
	v_and_b32_e32 v169, 0xffff0000, v129
	v_mul_f32_e32 v163, v163, v169
	v_lshlrev_b32_e32 v168, 16, v114
	v_fmac_f32_e32 v164, v173, v168
	v_and_b32_e32 v169, 0xffff0000, v114
	v_fmac_f32_e32 v165, v173, v169
	v_lshlrev_b32_e32 v168, 16, v130
	v_mul_f32_e32 v164, v164, v168
	v_and_b32_e32 v169, 0xffff0000, v130
	v_mul_f32_e32 v165, v165, v169
	v_lshlrev_b32_e32 v168, 16, v115
	v_fmac_f32_e32 v166, v173, v168
	v_and_b32_e32 v169, 0xffff0000, v115
	v_fmac_f32_e32 v167, v173, v169
	v_lshlrev_b32_e32 v168, 16, v131
	v_mul_f32_e32 v166, v166, v168
	v_and_b32_e32 v169, 0xffff0000, v131
	v_mul_f32_e32 v167, v167, v169
	v_cvt_pk_bf16_f32 v180, v160, v161
	v_cvt_pk_bf16_f32 v181, v162, v163
	v_cvt_pk_bf16_f32 v182, v164, v165
	v_cvt_pk_bf16_f32 v183, v166, v167
	global_store_dwordx4 v5, v[180:183], s[12:13]
	v_lshlrev_b32_e32 v168, 16, v84
	v_lshlrev_b32_e32 v169, 16, v100
	v_add_f32_e32 v160, v168, v169
	v_and_b32_e32 v168, 0xffff0000, v84
	v_and_b32_e32 v169, 0xffff0000, v100
	v_add_f32_e32 v161, v168, v169
	v_lshlrev_b32_e32 v168, 16, v85
	v_lshlrev_b32_e32 v169, 16, v101
	v_add_f32_e32 v162, v168, v169
	v_and_b32_e32 v168, 0xffff0000, v85
	v_and_b32_e32 v169, 0xffff0000, v101
	v_add_f32_e32 v163, v168, v169
	v_lshlrev_b32_e32 v168, 16, v86
	v_lshlrev_b32_e32 v169, 16, v102
	v_add_f32_e32 v164, v168, v169
	v_and_b32_e32 v168, 0xffff0000, v86
	v_and_b32_e32 v169, 0xffff0000, v102
	v_add_f32_e32 v165, v168, v169
	v_lshlrev_b32_e32 v168, 16, v87
	v_lshlrev_b32_e32 v169, 16, v103
	v_add_f32_e32 v166, v168, v169
	v_and_b32_e32 v168, 0xffff0000, v87
	v_and_b32_e32 v169, 0xffff0000, v103
	v_add_f32_e32 v167, v168, v169
	v_add_f32_e32 v170, v160, v161
	v_add_f32_e32 v170, v170, v162
	v_add_f32_e32 v170, v170, v163
	v_add_f32_e32 v170, v170, v164
	v_add_f32_e32 v170, v170, v165
	v_add_f32_e32 v170, v170, v166
	v_add_f32_e32 v170, v170, v167
	s_nop 1
	v_add_f32_dpp v170, v170, v170 quad_perm:[1,0,3,2] row_mask:0xf bank_mask:0xf bound_ctrl:1
	s_nop 1
	v_add_f32_dpp v170, v170, v170 quad_perm:[2,3,0,1] row_mask:0xf bank_mask:0xf bound_ctrl:1
	s_nop 1
	v_add_f32_dpp v170, v170, v170 row_half_mirror row_mask:0xf bank_mask:0xf bound_ctrl:1
	v_mul_f32_e32 v170, 0x3c800000, v170
	v_sub_f32_e32 v160, v160, v170
	v_sub_f32_e32 v161, v161, v170
	v_sub_f32_e32 v162, v162, v170
	v_sub_f32_e32 v163, v163, v170
	v_sub_f32_e32 v164, v164, v170
	v_sub_f32_e32 v165, v165, v170
	v_sub_f32_e32 v166, v166, v170
	v_sub_f32_e32 v167, v167, v170
	v_mul_f32_e32 v171, v160, v160
	v_fmac_f32_e32 v171, v161, v161
	v_fmac_f32_e32 v171, v162, v162
	v_fmac_f32_e32 v171, v163, v163
	v_fmac_f32_e32 v171, v164, v164
	v_fmac_f32_e32 v171, v165, v165
	v_fmac_f32_e32 v171, v166, v166
	v_fmac_f32_e32 v171, v167, v167
	s_nop 1
	v_add_f32_dpp v171, v171, v171 quad_perm:[1,0,3,2] row_mask:0xf bank_mask:0xf bound_ctrl:1
	s_nop 1
	v_add_f32_dpp v171, v171, v171 quad_perm:[2,3,0,1] row_mask:0xf bank_mask:0xf bound_ctrl:1
	s_nop 1
	v_add_f32_dpp v171, v171, v171 row_half_mirror row_mask:0xf bank_mask:0xf bound_ctrl:1
	v_mov_b32_e32 v172, 0x3a27c5ac
	v_fmac_f32_e32 v172, 0x3c800000, v171
	v_rsq_f32_e32 v172, v172
	v_add_f32_e32 v173, v145, v149
	s_nop 0
	v_mul_f32_e32 v160, v160, v172
	v_mul_f32_e32 v161, v161, v172
	v_mul_f32_e32 v162, v162, v172
	v_mul_f32_e32 v163, v163, v172
	v_mul_f32_e32 v164, v164, v172
	v_mul_f32_e32 v165, v165, v172
	v_mul_f32_e32 v166, v166, v172
	v_mul_f32_e32 v167, v167, v172
	v_fma_f32 v160, v18, v160, v50
	v_fma_f32 v161, v19, v161, v51
	v_fma_f32 v162, v20, v162, v52
	v_fma_f32 v163, v21, v163, v53
	v_fma_f32 v164, v22, v164, v54
	v_fma_f32 v165, v23, v165, v55
	v_fma_f32 v166, v24, v166, v56
	v_fma_f32 v167, v25, v167, v57
	v_lshlrev_b32_e32 v168, 16, v116
	v_fmac_f32_e32 v160, v173, v168
	v_and_b32_e32 v169, 0xffff0000, v116
	v_fmac_f32_e32 v161, v173, v169
	v_lshlrev_b32_e32 v168, 16, v132
	v_mul_f32_e32 v160, v160, v168
	v_and_b32_e32 v169, 0xffff0000, v132
	v_mul_f32_e32 v161, v161, v169
	v_lshlrev_b32_e32 v168, 16, v117
	v_fmac_f32_e32 v162, v173, v168
	v_and_b32_e32 v169, 0xffff0000, v117
	v_fmac_f32_e32 v163, v173, v169
	v_lshlrev_b32_e32 v168, 16, v133
	v_mul_f32_e32 v162, v162, v168
	v_and_b32_e32 v169, 0xffff0000, v133
	v_mul_f32_e32 v163, v163, v169
	v_lshlrev_b32_e32 v168, 16, v118
	v_fmac_f32_e32 v164, v173, v168
	v_and_b32_e32 v169, 0xffff0000, v118
	v_fmac_f32_e32 v165, v173, v169
	v_lshlrev_b32_e32 v168, 16, v134
	v_mul_f32_e32 v164, v164, v168
	v_and_b32_e32 v169, 0xffff0000, v134
	v_mul_f32_e32 v165, v165, v169
	v_lshlrev_b32_e32 v168, 16, v119
	v_fmac_f32_e32 v166, v173, v168
	v_and_b32_e32 v169, 0xffff0000, v119
	v_fmac_f32_e32 v167, v173, v169
	v_lshlrev_b32_e32 v168, 16, v135
	v_mul_f32_e32 v166, v166, v168
	v_and_b32_e32 v169, 0xffff0000, v135
	v_mul_f32_e32 v167, v167, v169
	v_cvt_pk_bf16_f32 v184, v160, v161
	v_cvt_pk_bf16_f32 v185, v162, v163
	v_cvt_pk_bf16_f32 v186, v164, v165
	v_cvt_pk_bf16_f32 v187, v166, v167
	global_store_dwordx4 v5, v[184:187], s[12:13] offset:1024
	v_lshlrev_b32_e32 v168, 16, v88
	v_lshlrev_b32_e32 v169, 16, v104
	v_add_f32_e32 v160, v168, v169
	v_and_b32_e32 v168, 0xffff0000, v88
	v_and_b32_e32 v169, 0xffff0000, v104
	v_add_f32_e32 v161, v168, v169
	v_lshlrev_b32_e32 v168, 16, v89
	v_lshlrev_b32_e32 v169, 16, v105
	v_add_f32_e32 v162, v168, v169
	v_and_b32_e32 v168, 0xffff0000, v89
	v_and_b32_e32 v169, 0xffff0000, v105
	v_add_f32_e32 v163, v168, v169
	v_lshlrev_b32_e32 v168, 16, v90
	v_lshlrev_b32_e32 v169, 16, v106
	v_add_f32_e32 v164, v168, v169
	v_and_b32_e32 v168, 0xffff0000, v90
	v_and_b32_e32 v169, 0xffff0000, v106
	v_add_f32_e32 v165, v168, v169
	v_lshlrev_b32_e32 v168, 16, v91
	v_lshlrev_b32_e32 v169, 16, v107
	v_add_f32_e32 v166, v168, v169
	v_and_b32_e32 v168, 0xffff0000, v91
	v_and_b32_e32 v169, 0xffff0000, v107
	v_add_f32_e32 v167, v168, v169
	v_add_f32_e32 v170, v160, v161
	v_add_f32_e32 v170, v170, v162
	v_add_f32_e32 v170, v170, v163
	v_add_f32_e32 v170, v170, v164
	v_add_f32_e32 v170, v170, v165
	v_add_f32_e32 v170, v170, v166
	v_add_f32_e32 v170, v170, v167
	s_nop 1
	v_add_f32_dpp v170, v170, v170 quad_perm:[1,0,3,2] row_mask:0xf bank_mask:0xf bound_ctrl:1
	s_nop 1
	v_add_f32_dpp v170, v170, v170 quad_perm:[2,3,0,1] row_mask:0xf bank_mask:0xf bound_ctrl:1
	s_nop 1
	v_add_f32_dpp v170, v170, v170 row_half_mirror row_mask:0xf bank_mask:0xf bound_ctrl:1
	v_mul_f32_e32 v170, 0x3c800000, v170
	v_sub_f32_e32 v160, v160, v170
	v_sub_f32_e32 v161, v161, v170
	v_sub_f32_e32 v162, v162, v170
	v_sub_f32_e32 v163, v163, v170
	v_sub_f32_e32 v164, v164, v170
	v_sub_f32_e32 v165, v165, v170
	v_sub_f32_e32 v166, v166, v170
	v_sub_f32_e32 v167, v167, v170
	v_mul_f32_e32 v171, v160, v160
	v_fmac_f32_e32 v171, v161, v161
	v_fmac_f32_e32 v171, v162, v162
	v_fmac_f32_e32 v171, v163, v163
	v_fmac_f32_e32 v171, v164, v164
	v_fmac_f32_e32 v171, v165, v165
	v_fmac_f32_e32 v171, v166, v166
	v_fmac_f32_e32 v171, v167, v167
	s_nop 1
	v_add_f32_dpp v171, v171, v171 quad_perm:[1,0,3,2] row_mask:0xf bank_mask:0xf bound_ctrl:1
	s_nop 1
	v_add_f32_dpp v171, v171, v171 quad_perm:[2,3,0,1] row_mask:0xf bank_mask:0xf bound_ctrl:1
	s_nop 1
	v_add_f32_dpp v171, v171, v171 row_half_mirror row_mask:0xf bank_mask:0xf bound_ctrl:1
	v_mov_b32_e32 v172, 0x3a27c5ac
	v_fmac_f32_e32 v172, 0x3c800000, v171
	v_rsq_f32_e32 v172, v172
	v_add_f32_e32 v173, v146, v150
	s_nop 0
	v_mul_f32_e32 v160, v160, v172
	v_mul_f32_e32 v161, v161, v172
	v_mul_f32_e32 v162, v162, v172
	v_mul_f32_e32 v163, v163, v172
	v_mul_f32_e32 v164, v164, v172
	v_mul_f32_e32 v165, v165, v172
	v_mul_f32_e32 v166, v166, v172
	v_mul_f32_e32 v167, v167, v172
	v_fma_f32 v160, v26, v160, v58
	v_fma_f32 v161, v27, v161, v59
	v_fma_f32 v162, v28, v162, v60
	v_fma_f32 v163, v29, v163, v61
	v_fma_f32 v164, v30, v164, v62
	v_fma_f32 v165, v31, v165, v63
	v_fma_f32 v166, v32, v166, v64
	v_fma_f32 v167, v33, v167, v65
	v_lshlrev_b32_e32 v168, 16, v120
	v_fmac_f32_e32 v160, v173, v168
	v_and_b32_e32 v169, 0xffff0000, v120
	v_fmac_f32_e32 v161, v173, v169
	v_lshlrev_b32_e32 v168, 16, v136
	v_mul_f32_e32 v160, v160, v168
	v_and_b32_e32 v169, 0xffff0000, v136
	v_mul_f32_e32 v161, v161, v169
	v_lshlrev_b32_e32 v168, 16, v121
	v_fmac_f32_e32 v162, v173, v168
	v_and_b32_e32 v169, 0xffff0000, v121
	v_fmac_f32_e32 v163, v173, v169
	v_lshlrev_b32_e32 v168, 16, v137
	v_mul_f32_e32 v162, v162, v168
	v_and_b32_e32 v169, 0xffff0000, v137
	v_mul_f32_e32 v163, v163, v169
	v_lshlrev_b32_e32 v168, 16, v122
	v_fmac_f32_e32 v164, v173, v168
	v_and_b32_e32 v169, 0xffff0000, v122
	v_fmac_f32_e32 v165, v173, v169
	v_lshlrev_b32_e32 v168, 16, v138
	v_mul_f32_e32 v164, v164, v168
	v_and_b32_e32 v169, 0xffff0000, v138
	v_mul_f32_e32 v165, v165, v169
	v_lshlrev_b32_e32 v168, 16, v123
	v_fmac_f32_e32 v166, v173, v168
	v_and_b32_e32 v169, 0xffff0000, v123
	v_fmac_f32_e32 v167, v173, v169
	v_lshlrev_b32_e32 v168, 16, v139
	v_mul_f32_e32 v166, v166, v168
	v_and_b32_e32 v169, 0xffff0000, v139
	v_mul_f32_e32 v167, v167, v169
	v_cvt_pk_bf16_f32 v192, v160, v161
	v_cvt_pk_bf16_f32 v193, v162, v163
	v_cvt_pk_bf16_f32 v194, v164, v165
	v_cvt_pk_bf16_f32 v195, v166, v167
	global_store_dwordx4 v5, v[192:195], s[12:13] offset:2048
	v_lshlrev_b32_e32 v168, 16, v92
	v_lshlrev_b32_e32 v169, 16, v108
	v_add_f32_e32 v160, v168, v169
	v_and_b32_e32 v168, 0xffff0000, v92
	v_and_b32_e32 v169, 0xffff0000, v108
	v_add_f32_e32 v161, v168, v169
	v_lshlrev_b32_e32 v168, 16, v93
	v_lshlrev_b32_e32 v169, 16, v109
	v_add_f32_e32 v162, v168, v169
	v_and_b32_e32 v168, 0xffff0000, v93
	v_and_b32_e32 v169, 0xffff0000, v109
	v_add_f32_e32 v163, v168, v169
	v_lshlrev_b32_e32 v168, 16, v94
	v_lshlrev_b32_e32 v169, 16, v110
	v_add_f32_e32 v164, v168, v169
	v_and_b32_e32 v168, 0xffff0000, v94
	v_and_b32_e32 v169, 0xffff0000, v110
	v_add_f32_e32 v165, v168, v169
	v_lshlrev_b32_e32 v168, 16, v95
	v_lshlrev_b32_e32 v169, 16, v111
	v_add_f32_e32 v166, v168, v169
	v_and_b32_e32 v168, 0xffff0000, v95
	v_and_b32_e32 v169, 0xffff0000, v111
	v_add_f32_e32 v167, v168, v169
	v_add_f32_e32 v170, v160, v161
	v_add_f32_e32 v170, v170, v162
	v_add_f32_e32 v170, v170, v163
	v_add_f32_e32 v170, v170, v164
	v_add_f32_e32 v170, v170, v165
	v_add_f32_e32 v170, v170, v166
	v_add_f32_e32 v170, v170, v167
	s_nop 1
	v_add_f32_dpp v170, v170, v170 quad_perm:[1,0,3,2] row_mask:0xf bank_mask:0xf bound_ctrl:1
	s_nop 1
	v_add_f32_dpp v170, v170, v170 quad_perm:[2,3,0,1] row_mask:0xf bank_mask:0xf bound_ctrl:1
	s_nop 1
	v_add_f32_dpp v170, v170, v170 row_half_mirror row_mask:0xf bank_mask:0xf bound_ctrl:1
	v_mul_f32_e32 v170, 0x3c800000, v170
	v_sub_f32_e32 v160, v160, v170
	v_sub_f32_e32 v161, v161, v170
	v_sub_f32_e32 v162, v162, v170
	v_sub_f32_e32 v163, v163, v170
	v_sub_f32_e32 v164, v164, v170
	v_sub_f32_e32 v165, v165, v170
	v_sub_f32_e32 v166, v166, v170
	v_sub_f32_e32 v167, v167, v170
	v_mul_f32_e32 v171, v160, v160
	v_fmac_f32_e32 v171, v161, v161
	v_fmac_f32_e32 v171, v162, v162
	v_fmac_f32_e32 v171, v163, v163
	v_fmac_f32_e32 v171, v164, v164
	v_fmac_f32_e32 v171, v165, v165
	v_fmac_f32_e32 v171, v166, v166
	v_fmac_f32_e32 v171, v167, v167
	s_nop 1
	v_add_f32_dpp v171, v171, v171 quad_perm:[1,0,3,2] row_mask:0xf bank_mask:0xf bound_ctrl:1
	s_nop 1
	v_add_f32_dpp v171, v171, v171 quad_perm:[2,3,0,1] row_mask:0xf bank_mask:0xf bound_ctrl:1
	s_nop 1
	v_add_f32_dpp v171, v171, v171 row_half_mirror row_mask:0xf bank_mask:0xf bound_ctrl:1
	v_mov_b32_e32 v172, 0x3a27c5ac
	v_fmac_f32_e32 v172, 0x3c800000, v171
	v_rsq_f32_e32 v172, v172
	v_add_f32_e32 v173, v147, v151
	s_nop 0
	v_mul_f32_e32 v160, v160, v172
	v_mul_f32_e32 v161, v161, v172
	v_mul_f32_e32 v162, v162, v172
	v_mul_f32_e32 v163, v163, v172
	v_mul_f32_e32 v164, v164, v172
	v_mul_f32_e32 v165, v165, v172
	v_mul_f32_e32 v166, v166, v172
	v_mul_f32_e32 v167, v167, v172
	v_fma_f32 v160, v34, v160, v66
	v_fma_f32 v161, v35, v161, v67
	v_fma_f32 v162, v36, v162, v68
	v_fma_f32 v163, v37, v163, v69
	v_fma_f32 v164, v38, v164, v70
	v_fma_f32 v165, v39, v165, v71
	v_fma_f32 v166, v40, v166, v72
	v_fma_f32 v167, v41, v167, v73
	v_lshlrev_b32_e32 v168, 16, v124
	v_fmac_f32_e32 v160, v173, v168
	v_and_b32_e32 v169, 0xffff0000, v124
	v_fmac_f32_e32 v161, v173, v169
	v_lshlrev_b32_e32 v168, 16, v140
	v_mul_f32_e32 v160, v160, v168
	v_and_b32_e32 v169, 0xffff0000, v140
	v_mul_f32_e32 v161, v161, v169
	v_lshlrev_b32_e32 v168, 16, v125
	v_fmac_f32_e32 v162, v173, v168
	v_and_b32_e32 v169, 0xffff0000, v125
	v_fmac_f32_e32 v163, v173, v169
	v_lshlrev_b32_e32 v168, 16, v141
	v_mul_f32_e32 v162, v162, v168
	v_and_b32_e32 v169, 0xffff0000, v141
	v_mul_f32_e32 v163, v163, v169
	v_lshlrev_b32_e32 v168, 16, v126
	v_fmac_f32_e32 v164, v173, v168
	v_and_b32_e32 v169, 0xffff0000, v126
	v_fmac_f32_e32 v165, v173, v169
	v_lshlrev_b32_e32 v168, 16, v142
	v_mul_f32_e32 v164, v164, v168
	v_and_b32_e32 v169, 0xffff0000, v142
	v_mul_f32_e32 v165, v165, v169
	v_lshlrev_b32_e32 v168, 16, v127
	v_fmac_f32_e32 v166, v173, v168
	v_and_b32_e32 v169, 0xffff0000, v127
	v_fmac_f32_e32 v167, v173, v169
	v_lshlrev_b32_e32 v168, 16, v143
	v_mul_f32_e32 v166, v166, v168
	v_and_b32_e32 v169, 0xffff0000, v143
	v_mul_f32_e32 v167, v167, v169
	v_cvt_pk_bf16_f32 v196, v160, v161
	v_cvt_pk_bf16_f32 v197, v162, v163
	v_cvt_pk_bf16_f32 v198, v164, v165
	v_cvt_pk_bf16_f32 v199, v166, v167
	global_store_dwordx4 v5, v[196:199], s[12:13] offset:3072
	s_add_i32 s24, s24, 1
	s_cmp_lt_u32 s24, 32
	s_cbranch_scc1 .Lx14_row
	s_waitcnt vmcnt(0)
	s_cmp_lg_u32 s82, 0
	s_cbranch_scc1 .Lx14_fin_other
	s_mov_b32 s27, 0
	v_mov_b32_e32 v5, 0x200
